# mixer retention path stage 2: the eight decay-table reads issued together and waited once
# speedup vs baseline: 1.0073x; 1.0073x over previous
.LBB0_474:
	s_andn2_b64 vcc, exec, s[8:9]
	s_cbranch_vccnz .LBB0_476
	s_add_i32 s5, 0, 0x1b200
	s_add_i32 s8, s5, s88
	v_mov_b32_e32 v73, s8
	ds_read_b128 v[200:203], v73
	s_add_i32 s8, s5, s89
	v_mov_b32_e32 v73, s8
	ds_read_b128 v[204:207], v73
	s_add_i32 s8, s5, s91
	v_mov_b32_e32 v73, s8
	ds_read_b128 v[208:211], v73
	s_add_i32 s8, s5, s28
	v_mov_b32_e32 v73, s8
	ds_read_b128 v[212:215], v73
	s_add_i32 s8, s5, s29
	v_mov_b32_e32 v73, s8
	ds_read_b128 v[220:223], v73
	s_add_i32 s8, s5, s96
	v_mov_b32_e32 v73, s8
	ds_read_b128 v[224:227], v73
	s_add_i32 s8, s5, s42
	v_mov_b32_e32 v73, s8
	ds_read_b128 v[232:235], v73
	s_add_i32 s8, s5, s43
	v_mov_b32_e32 v73, s8
	ds_read_b128 v[236:239], v73
	v_add_u32_e32 v73, s90, v108
	s_waitcnt lgkmcnt(0)
	v_pk_mul_f32 v[176:177], v[56:57], v[200:201] op_sel_hi:[1,0]
	v_mov_b32_e32 v178, v2
	v_mov_b32_e32 v179, v10
	v_pk_mul_f32 v[178:179], v[178:179], v[200:201] op_sel:[0,1]
	v_cvt_pk_bf16_f32 v176, v176, v177
	v_cvt_pk_bf16_f32 v178, v178, v179
	ds_write2st64_b32 v153, v176, v178 offset1:68
	v_pk_mul_f32 v[176:177], v[58:59], v[204:205] op_sel_hi:[1,0]
	v_mov_b32_e32 v178, v3
	v_mov_b32_e32 v179, v11
	v_pk_mul_f32 v[178:179], v[178:179], v[204:205] op_sel:[0,1]
	v_cvt_pk_bf16_f32 v176, v176, v177
	v_cvt_pk_bf16_f32 v178, v178, v179
	ds_write_b32 v73, v176
	ds_write_b32 v73, v178 offset:17408
	v_pk_mul_f32 v[176:177], v[60:61], v[208:209] op_sel_hi:[1,0]
	v_mov_b32_e32 v178, v4
	v_mov_b32_e32 v179, v12
	v_pk_mul_f32 v[178:179], v[178:179], v[208:209] op_sel:[0,1]
	v_cvt_pk_bf16_f32 v176, v176, v177
	v_cvt_pk_bf16_f32 v178, v178, v179
	ds_write_b32 v73, v176 offset:272
	ds_write_b32 v73, v178 offset:17680
	v_pk_mul_f32 v[176:177], v[62:63], v[212:213] op_sel_hi:[1,0]
	v_mov_b32_e32 v178, v5
	v_mov_b32_e32 v179, v13
	v_pk_mul_f32 v[178:179], v[178:179], v[212:213] op_sel:[0,1]
	v_cvt_pk_bf16_f32 v176, v176, v177
	v_cvt_pk_bf16_f32 v178, v178, v179
	ds_write_b32 v73, v176 offset:544
	ds_write_b32 v73, v178 offset:17952
	v_pk_mul_f32 v[176:177], v[64:65], v[220:221] op_sel_hi:[1,0]
	v_mov_b32_e32 v178, v6
	v_mov_b32_e32 v179, v14
	v_pk_mul_f32 v[178:179], v[178:179], v[220:221] op_sel:[0,1]
	v_cvt_pk_bf16_f32 v176, v176, v177
	v_cvt_pk_bf16_f32 v178, v178, v179
	ds_write_b32 v73, v176 offset:816
	ds_write_b32 v73, v178 offset:18224
	v_pk_mul_f32 v[176:177], v[66:67], v[224:225] op_sel_hi:[1,0]
	v_mov_b32_e32 v178, v7
	v_mov_b32_e32 v179, v15
	v_pk_mul_f32 v[178:179], v[178:179], v[224:225] op_sel:[0,1]
	v_cvt_pk_bf16_f32 v176, v176, v177
	v_cvt_pk_bf16_f32 v178, v178, v179
	ds_write_b32 v73, v176 offset:1088
	ds_write_b32 v73, v178 offset:18496
	v_pk_mul_f32 v[176:177], v[68:69], v[232:233] op_sel_hi:[1,0]
	v_mov_b32_e32 v178, v8
	v_mov_b32_e32 v179, v16
	v_pk_mul_f32 v[178:179], v[178:179], v[232:233] op_sel:[0,1]
	v_cvt_pk_bf16_f32 v176, v176, v177
	v_cvt_pk_bf16_f32 v178, v178, v179
	ds_write_b32 v73, v176 offset:1360
	ds_write_b32 v73, v178 offset:18768
	v_pk_mul_f32 v[176:177], v[70:71], v[236:237] op_sel_hi:[1,0]
	v_mov_b32_e32 v178, v9
	v_mov_b32_e32 v179, v17
	v_pk_mul_f32 v[178:179], v[178:179], v[236:237] op_sel:[0,1]
	v_cvt_pk_bf16_f32 v176, v176, v177
	v_cvt_pk_bf16_f32 v178, v178, v179
	ds_write_b32 v73, v176 offset:1632
	ds_write_b32 v73, v178 offset:19040
	v_mov_b32_e32 v206, v203
	s_nop 0
	v_pk_mul_f32 v[78:79], v[2:3], v[206:207]
	v_pk_mul_f32 v[80:81], v[10:11], v[206:207]
	v_mov_b32_e32 v214, v211
	s_nop 0
	v_pk_mul_f32 v[82:83], v[4:5], v[214:215]
	v_pk_mul_f32 v[84:85], v[12:13], v[214:215]
	v_mov_b32_e32 v226, v223
	s_nop 0
	v_pk_mul_f32 v[86:87], v[6:7], v[226:227]
	v_pk_mul_f32 v[88:89], v[14:15], v[226:227]
	v_mov_b32_e32 v238, v235
	s_nop 0
	v_pk_mul_f32 v[90:91], v[8:9], v[238:239]
	v_pk_mul_f32 v[92:93], v[16:17], v[238:239]
	v_mov_b32_e32 v74, v144
	v_mov_b32_e32 v75, v144
